# P14: routing records (expert, slot, gate) of the wave's four tokens prefetched as 12 dwordx4 before the token loop; per-token record loads and their waits removed
# baseline (speedup 1.0000x reference)
; #define LANE_NOW() ({ int l_ = lane_id_now(); asm volatile("" : "+v"(l_)); l_; })
; __global__ void __launch_bounds__(NTHR, 2) fwd(Args args) {
;     ...
;     if (IN(14)) {
;         const int lane = LANE_NOW(), tid = wave * 64 + lane; (void)tid; (void)lane;
;         const int gw = bx * NWAVES + wave, NGW = NG * NWAVES;
;         const unsigned* counts = ctl + CW_CNT;
;         int pb = 0;
;         { const int nb = (lane < E) ? (((int)counts[(lane & 31) * CNT_STRIDE] + 255) >> 8) : 0; int inc = nb;
; #pragma unroll
;           for (int o = 1; o < 32; o <<= 1) { const int v = __shfl_up(inc, o); if ((lane & 31) >= o) inc += v; }
;           pb = inc - nb; }
;         const float* X2 = WSP(float, WS_X2); const unsigned char* YK = WSP(unsigned char, WS_YK); const float* fn = INP(35); float* out = args.out;
;         f32x4 fg[8];
; #pragma unroll
;         for (int j = 0; j < 8; ++j) fg[j] = *(const f32x4*)(fn + (j * 64 + lane) * 4);
;         for (int t = gw; t < T; t += NGW) {
;             size_t so[TOPK]; float gk[TOPK];
; #pragma unroll
;             for (int k = 0; k < TOPK; ++k) { const int e = WSP(int, WS_SELE)[t * TOPK + k], p = WSP(int, WS_SELP)[t * TOPK + k]; gk[k] = WSP(float, WS_SELG)[t * TOPK + k] * Y8_INV;
;                 so[k] = ((size_t)__shfl(pb, e) * 256 + p) * D; }
.LBB0_1672:
	s_or_b64 exec, exec, s[0:1]
	s_waitcnt lgkmcnt(0)
	v_mbcnt_lo_u32_b32 v1, -1, 0
	v_mbcnt_hi_u32_b32 v32, -1, v1
	v_and_b32_e32 v86, 64, v32
	v_add_u32_e32 v1, -1, v32
	v_cmp_lt_i32_e32 vcc, v1, v86
	v_add_u32_e32 v3, -2, v32
	s_lshl_b32 s0, s92, 3
	v_cndmask_b32_e32 v1, v1, v32, vcc
	v_lshlrev_b32_e32 v1, 2, v1
	ds_bpermute_b32 v2, v1, v33
	v_and_b32_e32 v1, 31, v0
	v_cmp_ne_u32_e32 vcc, 0, v1
	s_add_i32 s0, s89, s0
	s_cmpk_gt_i32 s0, 0x1fff
	s_waitcnt lgkmcnt(0)
	v_cndmask_b32_e32 v2, 0, v2, vcc
	v_cmp_lt_i32_e32 vcc, v3, v86
	v_add_u32_e32 v2, v2, v33
	s_nop 0
	v_cndmask_b32_e32 v3, v3, v32, vcc
	v_lshlrev_b32_e32 v3, 2, v3
	ds_bpermute_b32 v3, v3, v2
	v_cmp_lt_u32_e32 vcc, 1, v1
	s_waitcnt lgkmcnt(0)
	s_nop 0
	v_cndmask_b32_e32 v3, 0, v3, vcc
	v_add_u32_e32 v2, v3, v2
	v_add_u32_e32 v3, -4, v32
	v_cmp_lt_i32_e32 vcc, v3, v86
	s_nop 1
	v_cndmask_b32_e32 v3, v3, v32, vcc
	v_lshlrev_b32_e32 v3, 2, v3
	ds_bpermute_b32 v3, v3, v2
	v_cmp_lt_u32_e32 vcc, 3, v1
	s_waitcnt lgkmcnt(0)
	s_nop 0
	v_cndmask_b32_e32 v3, 0, v3, vcc
	v_add_u32_e32 v2, v3, v2
	v_add_u32_e32 v3, -8, v32
	v_cmp_lt_i32_e32 vcc, v3, v86
	s_nop 1
	v_cndmask_b32_e32 v3, v3, v32, vcc
	v_lshlrev_b32_e32 v3, 2, v3
	ds_bpermute_b32 v3, v3, v2
	v_cmp_lt_u32_e32 vcc, 7, v1
	s_waitcnt lgkmcnt(0)
	s_nop 0
	v_cndmask_b32_e32 v3, 0, v3, vcc
	v_add_u32_e32 v34, v3, v2
	v_add_u32_e32 v2, -16, v32
	v_cmp_lt_i32_e32 vcc, v2, v86
	s_nop 1
	v_cndmask_b32_e32 v2, v2, v32, vcc
	v_lshlrev_b32_e32 v2, 2, v2
	ds_bpermute_b32 v2, v2, v34
	s_cbranch_scc1 .LBB0_1675
	v_lshlrev_b32_e32 v36, 2, v0
	v_ashrrev_i32_e32 v37, 31, v36
	v_lshlrev_b64 v[38:39], 2, v[36:37]
	v_add_u32_e32 v48, 0x400, v36
	v_add_u32_e32 v50, 0x500, v36
	v_add_u32_e32 v52, 0x600, v36
	v_cmp_lt_u32_e32 vcc, 15, v1
	v_lshl_add_u64 v[16:17], s[6:7], 0, v[38:39]
	v_ashrrev_i32_e32 v49, 31, v48
	v_ashrrev_i32_e32 v51, 31, v50
	v_ashrrev_i32_e32 v53, 31, v52
	v_add_u32_e32 v54, 0x700, v36
	s_waitcnt lgkmcnt(0)
	v_cndmask_b32_e32 v35, 0, v2, vcc
	global_load_dwordx4 v[0:3], v[16:17], off
	global_load_dwordx4 v[4:7], v[16:17], off offset:1024
	global_load_dwordx4 v[8:11], v[16:17], off offset:2048
	global_load_dwordx4 v[12:15], v[16:17], off offset:3072
	v_lshlrev_b64 v[68:69], 2, v[48:49]
	v_lshlrev_b64 v[70:71], 2, v[50:51]
	v_lshlrev_b64 v[72:73], 2, v[52:53]
	v_ashrrev_i32_e32 v55, 31, v54
	v_lshl_add_u64 v[24:25], s[6:7], 0, v[68:69]
	v_lshl_add_u64 v[26:27], s[6:7], 0, v[70:71]
	v_lshl_add_u64 v[40:41], s[6:7], 0, v[72:73]
	v_lshlrev_b64 v[74:75], 2, v[54:55]
	global_load_dwordx4 v[16:19], v[24:25], off
	global_load_dwordx4 v[20:23], v[26:27], off
	v_lshl_add_u64 v[42:43], s[6:7], 0, v[74:75]
	global_load_dwordx4 v[24:27], v[40:41], off
	global_load_dwordx4 v[28:31], v[42:43], off
	v_add_u32_e32 v40, v35, v34
	v_sub_u32_e32 v87, v40, v33
	v_add_u32_e32 v33, 64, v86
	v_xor_b32_e32 v40, 1, v32
	v_cmp_lt_i32_e32 vcc, v40, v33
	s_lshl_b32 s4, s83, 3
	s_add_u32 s2, s78, 0x2ddc8000
	v_cndmask_b32_e32 v40, v32, v40, vcc
	v_lshlrev_b32_e32 v88, 2, v40
	v_xor_b32_e32 v40, 2, v32
	v_cmp_lt_i32_e32 vcc, v40, v33
	s_addc_u32 s3, s79, 0
	v_add_u32_e32 v34, 0x100, v36
	v_cndmask_b32_e32 v40, v32, v40, vcc
	v_lshlrev_b32_e32 v89, 2, v40
	v_xor_b32_e32 v40, 4, v32
	v_cmp_lt_i32_e32 vcc, v40, v33
	v_add_u32_e32 v44, 0x200, v36
	v_add_u32_e32 v46, 0x300, v36
	v_cndmask_b32_e32 v40, v32, v40, vcc
	v_lshlrev_b32_e32 v90, 2, v40
	v_xor_b32_e32 v40, 8, v32
	v_cmp_lt_i32_e32 vcc, v40, v33
	s_add_u32 s12, s78, 0x23c68000
	v_ashrrev_i32_e32 v35, 31, v34
	v_cndmask_b32_e32 v40, v32, v40, vcc
	v_lshlrev_b32_e32 v91, 2, v40
	v_xor_b32_e32 v40, 16, v32
	v_cmp_lt_i32_e32 vcc, v40, v33
	v_ashrrev_i32_e32 v45, 31, v44
	v_ashrrev_i32_e32 v47, 31, v46
	v_cndmask_b32_e32 v40, v32, v40, vcc
	v_lshlrev_b32_e32 v92, 2, v40
	v_xor_b32_e32 v40, 32, v32
	v_cmp_lt_i32_e32 vcc, v40, v33
	s_addc_u32 s13, s79, 0
	s_add_u32 s14, s78, 0x23c88000
	v_cndmask_b32_e32 v32, v32, v40, vcc
	v_lshlrev_b32_e32 v93, 2, v32
	v_lshl_add_u64 v[40:41], s[2:3], 0, v[36:37]
	v_lshl_add_u64 v[42:43], s[2:3], 0, v[34:35]
	v_lshl_add_u64 v[44:45], s[2:3], 0, v[44:45]
	v_lshl_add_u64 v[46:47], s[2:3], 0, v[46:47]
	v_lshl_add_u64 v[48:49], s[2:3], 0, v[48:49]
	v_lshl_add_u64 v[50:51], s[2:3], 0, v[50:51]
	v_lshl_add_u64 v[52:53], s[2:3], 0, v[52:53]
	v_lshl_add_u64 v[54:55], s[2:3], 0, v[54:55]
	v_lshl_add_u64 v[32:33], s[78:79], 0, v[68:69]
	s_mov_b64 s[2:3], 0x1dc28000
	s_addc_u32 s15, s79, 0
	v_lshl_add_u64 v[58:59], v[32:33], 0, s[2:3]
	v_lshl_add_u64 v[32:33], s[78:79], 0, v[70:71]
	s_add_u32 s16, s78, 0x23ca8000
	v_lshl_add_u64 v[60:61], v[32:33], 0, s[2:3]
	v_lshl_add_u64 v[32:33], s[78:79], 0, v[72:73]
	s_addc_u32 s17, s79, 0
	s_ashr_i32 s1, s0, 31
	v_lshl_add_u64 v[62:63], v[32:33], 0, s[2:3]
	v_lshl_add_u64 v[32:33], s[78:79], 0, v[74:75]
	s_lshl_b64 s[6:7], s[0:1], 13
	v_lshl_add_u64 v[64:65], v[32:33], 0, s[2:3]
	s_lshl_b32 s1, s92, 5
	s_lshl_b32 s2, s89, 2
	s_ashr_i32 s5, s4, 31
	s_add_i32 s1, s1, s2
	v_lshl_add_u64 v[56:57], s[78:79], 0, v[38:39]
	s_lshl_b64 s[8:9], s[4:5], 13
	s_or_b32 s2, s1, 3
	s_lshl_b32 s1, s83, 5
	v_lshl_add_u64 v[66:67], s[76:77], 0, v[38:39]
	v_lshl_add_u64 v[68:69], s[76:77], 0, v[68:69]
	v_lshl_add_u64 v[70:71], s[76:77], 0, v[70:71]
	v_lshl_add_u64 v[72:73], s[76:77], 0, v[72:73]
	v_lshl_add_u64 v[74:75], s[76:77], 0, v[74:75]
	v_mov_b32_e32 v94, 0
	s_mov_b32 s5, 0x1dc28000
	v_mov_b32_e32 v95, 0x358637bd
	s_mov_b32 s18, 0x800000
	s_add_i32 s10, s2, -3
	s_lshl_b32 s10, s10, 2
	s_add_u32 s20, s12, s10
	s_addc_u32 s21, s13, 0
	global_load_dwordx4 v[184:187], v94, s[20:21]
	s_add_u32 s20, s14, s10
	s_addc_u32 s21, s15, 0
	global_load_dwordx4 v[188:191], v94, s[20:21]
	s_add_u32 s20, s16, s10
	s_addc_u32 s21, s17, 0
	global_load_dwordx4 v[192:195], v94, s[20:21]
	s_add_i32 s10, s2, 0x1ffd
	s_lshl_b32 s10, s10, 2
	s_add_u32 s20, s12, s10
	s_addc_u32 s21, s13, 0
	global_load_dwordx4 v[196:199], v94, s[20:21]
	s_add_u32 s20, s14, s10
	s_addc_u32 s21, s15, 0
	global_load_dwordx4 v[200:203], v94, s[20:21]
	s_add_u32 s20, s16, s10
	s_addc_u32 s21, s17, 0
	global_load_dwordx4 v[204:207], v94, s[20:21]
	s_add_i32 s10, s2, 0x3ffd
	s_lshl_b32 s10, s10, 2
	s_add_u32 s20, s12, s10
	s_addc_u32 s21, s13, 0
	global_load_dwordx4 v[208:211], v94, s[20:21]
	s_add_u32 s20, s14, s10
	s_addc_u32 s21, s15, 0
	global_load_dwordx4 v[212:215], v94, s[20:21]
	s_add_u32 s20, s16, s10
	s_addc_u32 s21, s17, 0
	global_load_dwordx4 v[216:219], v94, s[20:21]
	s_add_i32 s10, s2, 0x5ffd
	s_lshl_b32 s10, s10, 2
	s_add_u32 s20, s12, s10
	s_addc_u32 s21, s13, 0
	global_load_dwordx4 v[220:223], v94, s[20:21]
	s_add_u32 s20, s14, s10
	s_addc_u32 s21, s15, 0
	global_load_dwordx4 v[224:227], v94, s[20:21]
	s_add_u32 s20, s16, s10
	s_addc_u32 s21, s17, 0
	global_load_dwordx4 v[228:231], v94, s[20:21]
; __global__ void __launch_bounds__(NTHR, 2) fwd(Args args) {
;     ...
;         for (int t = gw; t < T; t += NGW) {
;             size_t so[TOPK]; float gk[TOPK];
; #pragma unroll
;             for (int k = 0; k < TOPK; ++k) { const int e = WSP(int, WS_SELE)[t * TOPK + k], p = WSP(int, WS_SELP)[t * TOPK + k]; gk[k] = WSP(float, WS_SELG)[t * TOPK + k] * Y8_INV;
;                 so[k] = ((size_t)__shfl(pb, e) * 256 + p) * D; }
;             f32x4 v[8]; float s = 0.f;
; #pragma unroll
;             for (int j = 0; j < 8; ++j) { const int cidx = (j * 64 + lane) * 4; f32x4 a = *(const f32x4*)(X2 + (size_t)t * D + cidx);
; #pragma unroll
;                 for (int k = 0; k < TOPK; ++k) { const unsigned y = *(const unsigned*)(YK + so[k] + cidx); const v2f lo = __builtin_amdgcn_cvt_pk_f32_fp8(y, false), hi = __builtin_amdgcn_cvt_pk_f32_fp8(y, true);
;                     a[0] += gk[k] * lo[0]; a[1] += gk[k] * lo[1]; a[2] += gk[k] * hi[0]; a[3] += gk[k] * hi[1]; }
;                 v[j] = a; s += (a[0] * a[0] + a[1] * a[1]) + (a[2] * a[2] + a[3] * a[3]); }
.LBB0_1674:
	s_add_i32 s10, s2, -3
	s_ashr_i32 s11, s10, 31
	v_lshl_add_u64 v[32:33], v[56:57], 0, s[6:7]
	s_lshl_b64 s[10:11], s[10:11], 2
	v_add_co_u32_e32 v120, vcc, s5, v32
	s_add_u32 s20, s12, s10
	v_lshl_add_u64 v[34:35], v[58:59], 0, s[6:7]
	v_lshl_add_u64 v[36:37], v[60:61], 0, s[6:7]
	v_lshl_add_u64 v[38:39], v[62:63], 0, s[6:7]
	v_lshl_add_u64 v[112:113], v[64:65], 0, s[6:7]
	v_addc_co_u32_e32 v121, vcc, 0, v33, vcc
	s_addc_u32 s21, s13, s11
	global_load_dwordx4 v[96:99], v[34:35], off
	global_load_dwordx4 v[100:103], v[36:37], off
	global_load_dwordx4 v[104:107], v[38:39], off
	global_load_dwordx4 v[108:111], v[112:113], off
	s_nop 0
	global_load_dwordx4 v[112:115], v[120:121], off
	global_load_dwordx4 v[36:39], v[120:121], off offset:1024
	global_load_dwordx4 v[116:119], v[120:121], off offset:2048
	global_load_dwordx4 v[32:35], v[120:121], off offset:3072
	v_lshl_add_u64 v[76:77], v[66:67], 0, s[6:7]
	s_waitcnt vmcnt(16)
	v_mov_b32_e32 v121, v184
	s_add_u32 s20, s14, s10
	s_addc_u32 s21, s15, s11
	s_add_u32 s10, s16, s10
	s_addc_u32 s11, s17, s11
	v_mov_b32_e32 v120, v188
	v_mov_b32_e32 v123, v192
	s_add_i32 s20, s2, -2
	s_ashr_i32 s21, s20, 31
	s_lshl_b64 s[10:11], s[20:21], 2
	s_add_u32 s20, s12, s10
	s_addc_u32 s21, s13, s11
	v_mov_b32_e32 v125, v185
	s_add_u32 s20, s14, s10
	s_addc_u32 s21, s15, s11
	s_add_u32 s10, s16, s10
	s_addc_u32 s11, s17, s11
	v_mov_b32_e32 v122, v189
	v_mov_b32_e32 v127, v193
	s_add_i32 s20, s2, -1
	s_ashr_i32 s21, s20, 31
	s_lshl_b64 s[10:11], s[20:21], 2
	s_add_u32 s20, s12, s10
	s_addc_u32 s21, s13, s11
	v_mov_b32_e32 v131, v186
	s_add_u32 s20, s14, s10
	s_addc_u32 s21, s15, s11
	s_add_u32 s10, s16, s10
	s_addc_u32 s11, s17, s11
	s_ashr_i32 s3, s2, 31
	v_mov_b32_e32 v124, v190
	v_mov_b32_e32 v150, v194
	s_lshl_b64 s[10:11], s[2:3], 2
	s_add_u32 s20, s12, s10
	s_addc_u32 s21, s13, s11
	v_mov_b32_e32 v151, v187
	s_add_u32 s20, s14, s10
	s_addc_u32 s21, s15, s11
	v_mov_b32_e32 v126, v191
	s_add_u32 s10, s16, s10
	s_addc_u32 s11, s17, s11
	v_mov_b32_e32 v154, v195
	s_add_i32 s0, s0, s4
	s_add_i32 s2, s2, s1
	v_lshl_add_u64 v[78:79], v[68:69], 0, s[6:7]
	v_lshl_add_u64 v[80:81], v[70:71], 0, s[6:7]
	v_lshl_add_u64 v[82:83], v[72:73], 0, s[6:7]
	v_lshl_add_u64 v[84:85], v[74:75], 0, s[6:7]
	v_lshl_add_u64 v[56:57], v[56:57], 0, s[8:9]
	v_lshl_add_u64 v[58:59], v[58:59], 0, s[8:9]
	v_lshl_add_u64 v[60:61], v[60:61], 0, s[8:9]
	v_lshl_add_u64 v[62:63], v[62:63], 0, s[8:9]
	v_lshl_add_u64 v[64:65], v[64:65], 0, s[8:9]
	v_lshl_add_u64 v[66:67], v[66:67], 0, s[8:9]
	v_lshl_add_u64 v[68:69], v[68:69], 0, s[8:9]
	v_lshl_add_u64 v[70:71], v[70:71], 0, s[8:9]
	v_lshl_add_u64 v[72:73], v[72:73], 0, s[8:9]
	v_lshl_add_u64 v[74:75], v[74:75], 0, s[8:9]
	s_cmpk_lt_i32 s0, 0x2000
	v_and_or_b32 v121, v121, 63, v86
	v_lshlrev_b32_e32 v121, 2, v121
	ds_bpermute_b32 v128, v121, v87
	v_ashrrev_i32_e32 v121, 31, v120
	v_mul_f32_e32 v130, 0x3d000000, v123
	s_waitcnt lgkmcnt(0)
	v_ashrrev_i32_e32 v129, 31, v128
	v_lshlrev_b64 v[120:121], 11, v[120:121]
	v_lshlrev_b64 v[128:129], 19, v[128:129]
	v_lshl_add_u64 v[120:121], v[128:129], 0, v[120:121]
	v_lshl_add_u64 v[132:133], v[40:41], 0, v[120:121]
	v_and_or_b32 v123, v125, 63, v86
	v_lshlrev_b32_e32 v125, 2, v123
	ds_bpermute_b32 v128, v125, v87
	v_lshl_add_u64 v[134:135], v[42:43], 0, v[120:121]
	v_lshl_add_u64 v[136:137], v[44:45], 0, v[120:121]
	v_ashrrev_i32_e32 v123, 31, v122
	v_lshl_add_u64 v[138:139], v[46:47], 0, v[120:121]
	v_lshl_add_u64 v[140:141], v[48:49], 0, v[120:121]
	v_lshl_add_u64 v[142:143], v[50:51], 0, v[120:121]
	v_lshl_add_u64 v[144:145], v[52:53], 0, v[120:121]
	v_lshl_add_u64 v[120:121], v[54:55], 0, v[120:121]
	global_load_dword v156, v[132:133], off
	global_load_dword v157, v[136:137], off
	s_waitcnt lgkmcnt(0)
	v_ashrrev_i32_e32 v129, 31, v128
	v_and_or_b32 v125, v131, 63, v86
	v_lshlrev_b64 v[122:123], 11, v[122:123]
	global_load_dword v158, v[140:141], off
	global_load_dword v159, v[142:143], off
	global_load_dword v160, v[144:145], off
	s_nop 0
	global_load_dword v121, v[120:121], off
	v_mul_f32_e32 v120, 0x3d000000, v127
	v_lshlrev_b64 v[128:129], 19, v[128:129]
	v_lshlrev_b32_e32 v127, 2, v125
	v_lshl_add_u64 v[122:123], v[128:129], 0, v[122:123]
	ds_bpermute_b32 v128, v127, v87
	v_lshl_add_u64 v[132:133], v[40:41], 0, v[122:123]
	global_load_dword v131, v[132:133], off
	v_lshl_add_u64 v[136:137], v[42:43], 0, v[122:123]
	v_lshl_add_u64 v[140:141], v[44:45], 0, v[122:123]
	v_lshl_add_u64 v[142:143], v[46:47], 0, v[122:123]
	v_lshl_add_u64 v[144:145], v[48:49], 0, v[122:123]
	v_lshl_add_u64 v[146:147], v[50:51], 0, v[122:123]
	v_lshl_add_u64 v[148:149], v[52:53], 0, v[122:123]
	v_lshl_add_u64 v[122:123], v[54:55], 0, v[122:123]
	v_ashrrev_i32_e32 v125, 31, v124
	global_load_dword v161, v[140:141], off
	global_load_dword v162, v[144:145], off
	global_load_dword v163, v[146:147], off
	global_load_dword v164, v[148:149], off
	s_nop 0
	global_load_dword v123, v[122:123], off
	s_waitcnt lgkmcnt(0)
	v_ashrrev_i32_e32 v129, 31, v128
	v_lshlrev_b64 v[124:125], 11, v[124:125]
	v_and_or_b32 v127, v151, 63, v86
	v_lshlrev_b64 v[128:129], 19, v[128:129]
	v_lshlrev_b32_e32 v132, 2, v127
	v_lshl_add_u64 v[124:125], v[128:129], 0, v[124:125]
	ds_bpermute_b32 v128, v132, v87
	v_lshl_add_u64 v[132:133], v[40:41], 0, v[124:125]
	v_lshl_add_u64 v[144:145], v[44:45], 0, v[124:125]
	v_mul_f32_e32 v122, 0x3d000000, v150
	v_lshl_add_u64 v[140:141], v[42:43], 0, v[124:125]
	v_lshl_add_u64 v[146:147], v[46:47], 0, v[124:125]
	v_lshl_add_u64 v[148:149], v[48:49], 0, v[124:125]
	v_lshl_add_u64 v[150:151], v[50:51], 0, v[124:125]
	v_lshl_add_u64 v[152:153], v[52:53], 0, v[124:125]
	v_lshl_add_u64 v[124:125], v[54:55], 0, v[124:125]
	global_load_dword v133, v[132:133], off
	s_nop 0
	global_load_dword v165, v[144:145], off
	global_load_dword v166, v[148:149], off
	global_load_dword v167, v[150:151], off
	global_load_dword v168, v[152:153], off
	global_load_dword v169, v[124:125], off
	v_ashrrev_i32_e32 v127, 31, v126
	s_waitcnt lgkmcnt(0)
; __global__ void __launch_bounds__(NTHR, 2) fwd(Args args) {
;     ...
;             for (int k = 0; k < TOPK; ++k) { const int e = WSP(int, WS_SELE)[t * TOPK + k], p = WSP(int, WS_SELP)[t * TOPK + k]; gk[k] = WSP(float, WS_SELG)[t * TOPK + k] * Y8_INV;
;                 so[k] = ((size_t)__shfl(pb, e) * 256 + p) * D; }
;             f32x4 v[8]; float s = 0.f;
; #pragma unroll
;             for (int j = 0; j < 8; ++j) { const int cidx = (j * 64 + lane) * 4; f32x4 a = *(const f32x4*)(X2 + (size_t)t * D + cidx);
; #pragma unroll
;                 for (int k = 0; k < TOPK; ++k) { const unsigned y = *(const unsigned*)(YK + so[k] + cidx); const v2f lo = __builtin_amdgcn_cvt_pk_f32_fp8(y, false), hi = __builtin_amdgcn_cvt_pk_f32_fp8(y, true);
;                     a[0] += gk[k] * lo[0]; a[1] += gk[k] * lo[1]; a[2] += gk[k] * hi[0]; a[3] += gk[k] * hi[1]; }
;                 v[j] = a; s += (a[0] * a[0] + a[1] * a[1]) + (a[2] * a[2] + a[3] * a[3]); }
	v_ashrrev_i32_e32 v129, 31, v128
	v_lshlrev_b64 v[126:127], 11, v[126:127]
	v_lshlrev_b64 v[124:125], 19, v[128:129]
	v_lshl_add_u64 v[124:125], v[124:125], 0, v[126:127]
	v_lshl_add_u64 v[126:127], v[40:41], 0, v[124:125]
	v_mul_f32_e32 v132, 0x3d000000, v154
	v_lshl_add_u64 v[128:129], v[42:43], 0, v[124:125]
	v_lshl_add_u64 v[144:145], v[44:45], 0, v[124:125]
	v_lshl_add_u64 v[148:149], v[46:47], 0, v[124:125]
	v_lshl_add_u64 v[150:151], v[48:49], 0, v[124:125]
	v_lshl_add_u64 v[152:153], v[50:51], 0, v[124:125]
	v_lshl_add_u64 v[154:155], v[52:53], 0, v[124:125]
	v_lshl_add_u64 v[124:125], v[54:55], 0, v[124:125]
	global_load_dword v170, v[126:127], off
	global_load_dword v171, v[134:135], off
	global_load_dword v172, v[136:137], off
	global_load_dword v173, v[140:141], off
	global_load_dword v174, v[128:129], off
	global_load_dword v175, v[144:145], off
	global_load_dword v176, v[138:139], off
	global_load_dword v177, v[142:143], off
	global_load_dword v178, v[146:147], off
	global_load_dword v179, v[148:149], off
	global_load_dword v180, v[150:151], off
	global_load_dword v181, v[152:153], off
	global_load_dword v182, v[154:155], off
	global_load_dword v183, v[124:125], off
	s_waitcnt vmcnt(31)
	v_cvt_pk_f32_fp8_e32 v[124:125], v156
	s_waitcnt vmcnt(30)
	v_cvt_pk_f32_fp8_e32 v[128:129], v157
	v_cvt_pk_f32_fp8_sdwa v[134:135], v157 src0_sel:WORD_1
	s_waitcnt vmcnt(29)
	v_cvt_pk_f32_fp8_e32 v[136:137], v158
	v_cvt_pk_f32_fp8_sdwa v[138:139], v158 src0_sel:WORD_1
	s_waitcnt vmcnt(28)
	v_cvt_pk_f32_fp8_e32 v[140:141], v159
	v_cvt_pk_f32_fp8_sdwa v[142:143], v159 src0_sel:WORD_1
	v_cvt_pk_f32_fp8_sdwa v[126:127], v156 src0_sel:WORD_1
	s_waitcnt vmcnt(27)
	v_cvt_pk_f32_fp8_e32 v[144:145], v160
	v_cvt_pk_f32_fp8_sdwa v[146:147], v160 src0_sel:WORD_1
	s_waitcnt vmcnt(26)
	v_cvt_pk_f32_fp8_e32 v[148:149], v121
	v_cvt_pk_f32_fp8_sdwa v[150:151], v121 src0_sel:WORD_1
	s_waitcnt vmcnt(25)
	v_pk_fma_f32 v[116:117], v[128:129], v[130:131], v[116:117] op_sel_hi:[1,0,1]
	v_pk_fma_f32 v[118:119], v[130:131], v[134:135], v[118:119] op_sel_hi:[0,1,1]
	v_pk_fma_f32 v[96:97], v[136:137], v[130:131], v[96:97] op_sel_hi:[1,0,1]
	v_pk_fma_f32 v[98:99], v[130:131], v[138:139], v[98:99] op_sel_hi:[0,1,1]
	v_pk_fma_f32 v[100:101], v[140:141], v[130:131], v[100:101] op_sel_hi:[1,0,1]
	s_waitcnt vmcnt(24)
	v_cvt_pk_f32_fp8_e32 v[128:129], v161
	v_cvt_pk_f32_fp8_sdwa v[134:135], v161 src0_sel:WORD_1
	s_waitcnt vmcnt(23)
	v_cvt_pk_f32_fp8_e32 v[136:137], v162
	v_cvt_pk_f32_fp8_sdwa v[138:139], v162 src0_sel:WORD_1
	v_pk_fma_f32 v[102:103], v[130:131], v[142:143], v[102:103] op_sel_hi:[0,1,1]
	s_waitcnt vmcnt(22)
	v_cvt_pk_f32_fp8_e32 v[140:141], v163
	v_cvt_pk_f32_fp8_sdwa v[142:143], v163 src0_sel:WORD_1
	v_pk_fma_f32 v[112:113], v[124:125], v[130:131], v[112:113] op_sel_hi:[1,0,1]
	v_pk_fma_f32 v[114:115], v[130:131], v[126:127], v[114:115] op_sel_hi:[0,1,1]
	v_pk_fma_f32 v[104:105], v[144:145], v[130:131], v[104:105] op_sel_hi:[1,0,1]
	v_pk_fma_f32 v[106:107], v[130:131], v[146:147], v[106:107] op_sel_hi:[0,1,1]
	v_pk_fma_f32 v[108:109], v[148:149], v[130:131], v[108:109] op_sel_hi:[1,0,1]
	v_pk_fma_f32 v[110:111], v[130:131], v[150:151], v[110:111] op_sel_hi:[0,1,1]
	v_cvt_pk_f32_fp8_e32 v[124:125], v131
	v_cvt_pk_f32_fp8_sdwa v[126:127], v131 src0_sel:WORD_1
	s_waitcnt vmcnt(21)
	v_cvt_pk_f32_fp8_e32 v[144:145], v164
	v_cvt_pk_f32_fp8_sdwa v[146:147], v164 src0_sel:WORD_1
	s_waitcnt vmcnt(20)
	v_cvt_pk_f32_fp8_e32 v[148:149], v123
	v_cvt_pk_f32_fp8_sdwa v[150:151], v123 src0_sel:WORD_1
	v_pk_fma_f32 v[116:117], v[128:129], v[120:121], v[116:117] op_sel_hi:[1,0,1]
	v_pk_fma_f32 v[118:119], v[120:121], v[134:135], v[118:119] op_sel_hi:[0,1,1]
	s_waitcnt vmcnt(18)
	v_cvt_pk_f32_fp8_e32 v[128:129], v165
	v_cvt_pk_f32_fp8_sdwa v[134:135], v165 src0_sel:WORD_1
	v_pk_fma_f32 v[96:97], v[136:137], v[120:121], v[96:97] op_sel_hi:[1,0,1]
	v_pk_fma_f32 v[98:99], v[120:121], v[138:139], v[98:99] op_sel_hi:[0,1,1]
	s_waitcnt vmcnt(17)
	v_cvt_pk_f32_fp8_e32 v[136:137], v166
	v_cvt_pk_f32_fp8_sdwa v[138:139], v166 src0_sel:WORD_1
	v_pk_fma_f32 v[100:101], v[140:141], v[120:121], v[100:101] op_sel_hi:[1,0,1]
	v_pk_fma_f32 v[102:103], v[120:121], v[142:143], v[102:103] op_sel_hi:[0,1,1]
	s_waitcnt vmcnt(16)
	v_cvt_pk_f32_fp8_e32 v[140:141], v167
	v_cvt_pk_f32_fp8_sdwa v[142:143], v167 src0_sel:WORD_1
	v_pk_fma_f32 v[112:113], v[124:125], v[120:121], v[112:113] op_sel_hi:[1,0,1]
	v_pk_fma_f32 v[114:115], v[120:121], v[126:127], v[114:115] op_sel_hi:[0,1,1]
	v_pk_fma_f32 v[104:105], v[144:145], v[120:121], v[104:105] op_sel_hi:[1,0,1]
	v_pk_fma_f32 v[106:107], v[120:121], v[146:147], v[106:107] op_sel_hi:[0,1,1]
	v_pk_fma_f32 v[108:109], v[148:149], v[120:121], v[108:109] op_sel_hi:[1,0,1]
	v_pk_fma_f32 v[110:111], v[120:121], v[150:151], v[110:111] op_sel_hi:[0,1,1]
	v_cvt_pk_f32_fp8_e32 v[124:125], v133
	v_cvt_pk_f32_fp8_sdwa v[126:127], v133 src0_sel:WORD_1
	s_waitcnt vmcnt(15)
	v_cvt_pk_f32_fp8_e32 v[144:145], v168
	v_cvt_pk_f32_fp8_sdwa v[146:147], v168 src0_sel:WORD_1
	s_waitcnt vmcnt(14)
	v_cvt_pk_f32_fp8_e32 v[148:149], v169
	v_cvt_pk_f32_fp8_sdwa v[150:151], v169 src0_sel:WORD_1
	v_pk_fma_f32 v[116:117], v[128:129], v[122:123], v[116:117] op_sel_hi:[1,0,1]
	v_pk_fma_f32 v[118:119], v[122:123], v[134:135], v[118:119] op_sel_hi:[0,1,1]
	s_waitcnt vmcnt(12)
	v_cvt_pk_f32_fp8_e32 v[128:129], v171
	v_cvt_pk_f32_fp8_sdwa v[134:135], v171 src0_sel:WORD_1
	v_pk_fma_f32 v[96:97], v[136:137], v[122:123], v[96:97] op_sel_hi:[1,0,1]
	v_pk_fma_f32 v[98:99], v[122:123], v[138:139], v[98:99] op_sel_hi:[0,1,1]
	s_waitcnt vmcnt(11)
; __global__ void __launch_bounds__(NTHR, 2) fwd(Args args) {
;     ...
;             f32x4 v[8]; float s = 0.f;
; #pragma unroll
;             for (int j = 0; j < 8; ++j) { const int cidx = (j * 64 + lane) * 4; f32x4 a = *(const f32x4*)(X2 + (size_t)t * D + cidx);
; #pragma unroll
;                 for (int k = 0; k < TOPK; ++k) { const unsigned y = *(const unsigned*)(YK + so[k] + cidx); const v2f lo = __builtin_amdgcn_cvt_pk_f32_fp8(y, false), hi = __builtin_amdgcn_cvt_pk_f32_fp8(y, true);
;                     a[0] += gk[k] * lo[0]; a[1] += gk[k] * lo[1]; a[2] += gk[k] * hi[0]; a[3] += gk[k] * hi[1]; }
;                 v[j] = a; s += (a[0] * a[0] + a[1] * a[1]) + (a[2] * a[2] + a[3] * a[3]); }
;             const float r = rsqrtf(wave_sum(s) * (1.f / D) + EPS);
	v_cvt_pk_f32_fp8_e32 v[136:137], v172
	v_cvt_pk_f32_fp8_sdwa v[138:139], v172 src0_sel:WORD_1
	v_pk_fma_f32 v[100:101], v[140:141], v[122:123], v[100:101] op_sel_hi:[1,0,1]
	v_pk_fma_f32 v[102:103], v[122:123], v[142:143], v[102:103] op_sel_hi:[0,1,1]
	s_waitcnt vmcnt(10)
	v_cvt_pk_f32_fp8_e32 v[140:141], v173
	v_cvt_pk_f32_fp8_sdwa v[142:143], v173 src0_sel:WORD_1
	v_pk_fma_f32 v[112:113], v[124:125], v[122:123], v[112:113] op_sel_hi:[1,0,1]
	v_pk_fma_f32 v[114:115], v[122:123], v[126:127], v[114:115] op_sel_hi:[0,1,1]
	v_pk_fma_f32 v[104:105], v[144:145], v[122:123], v[104:105] op_sel_hi:[1,0,1]
	v_pk_fma_f32 v[106:107], v[122:123], v[146:147], v[106:107] op_sel_hi:[0,1,1]
	v_pk_fma_f32 v[108:109], v[148:149], v[122:123], v[108:109] op_sel_hi:[1,0,1]
	v_pk_fma_f32 v[110:111], v[122:123], v[150:151], v[110:111] op_sel_hi:[0,1,1]
	v_cvt_pk_f32_fp8_e32 v[124:125], v170
	v_cvt_pk_f32_fp8_sdwa v[126:127], v170 src0_sel:WORD_1
	s_waitcnt vmcnt(9)
	v_cvt_pk_f32_fp8_e32 v[144:145], v174
	v_cvt_pk_f32_fp8_sdwa v[146:147], v174 src0_sel:WORD_1
	s_waitcnt vmcnt(8)
	v_cvt_pk_f32_fp8_e32 v[148:149], v175
	v_cvt_pk_f32_fp8_sdwa v[150:151], v175 src0_sel:WORD_1
	s_waitcnt vmcnt(7)
	v_cvt_pk_f32_fp8_e32 v[152:153], v176
	v_cvt_pk_f32_fp8_sdwa v[154:155], v176 src0_sel:WORD_1
	s_waitcnt vmcnt(6)
	v_cvt_pk_f32_fp8_e32 v[156:157], v177
	v_cvt_pk_f32_fp8_sdwa v[158:159], v177 src0_sel:WORD_1
	v_pk_fma_f32 v[36:37], v[128:129], v[130:131], v[36:37] op_sel_hi:[1,0,1]
	v_pk_fma_f32 v[38:39], v[130:131], v[134:135], v[38:39] op_sel_hi:[0,1,1]
	s_waitcnt vmcnt(5)
	v_cvt_pk_f32_fp8_e32 v[160:161], v178
	v_cvt_pk_f32_fp8_sdwa v[162:163], v178 src0_sel:WORD_1
	v_pk_fma_f32 v[36:37], v[136:137], v[120:121], v[36:37] op_sel_hi:[1,0,1]
	v_pk_fma_f32 v[38:39], v[120:121], v[138:139], v[38:39] op_sel_hi:[0,1,1]
	s_waitcnt vmcnt(4)
	v_cvt_pk_f32_fp8_e32 v[164:165], v179
	v_cvt_pk_f32_fp8_sdwa v[166:167], v179 src0_sel:WORD_1
	v_pk_fma_f32 v[36:37], v[140:141], v[122:123], v[36:37] op_sel_hi:[1,0,1]
	v_pk_fma_f32 v[38:39], v[122:123], v[142:143], v[38:39] op_sel_hi:[0,1,1]
	s_waitcnt vmcnt(3)
	v_cvt_pk_f32_fp8_e32 v[168:169], v180
	v_cvt_pk_f32_fp8_sdwa v[170:171], v180 src0_sel:WORD_1
	s_waitcnt vmcnt(2)
	v_cvt_pk_f32_fp8_e32 v[172:173], v181
	v_cvt_pk_f32_fp8_sdwa v[174:175], v181 src0_sel:WORD_1
	s_waitcnt vmcnt(1)
	v_cvt_pk_f32_fp8_e32 v[176:177], v182
	v_cvt_pk_f32_fp8_sdwa v[178:179], v182 src0_sel:WORD_1
	s_waitcnt vmcnt(0)
	v_cvt_pk_f32_fp8_e32 v[180:181], v183
	v_cvt_pk_f32_fp8_sdwa v[182:183], v183 src0_sel:WORD_1
	v_pk_fma_f32 v[112:113], v[124:125], v[132:133], v[112:113] op_sel_hi:[1,0,1]
	v_pk_fma_f32 v[114:115], v[132:133], v[126:127], v[114:115] op_sel_hi:[0,1,1]
	v_pk_fma_f32 v[116:117], v[148:149], v[132:133], v[116:117] op_sel_hi:[1,0,1]
	v_pk_fma_f32 v[118:119], v[132:133], v[150:151], v[118:119] op_sel_hi:[0,1,1]
	v_pk_fma_f32 v[32:33], v[152:153], v[130:131], v[32:33] op_sel_hi:[1,0,1]
	v_pk_fma_f32 v[34:35], v[130:131], v[154:155], v[34:35] op_sel_hi:[0,1,1]
	v_pk_fma_f32 v[36:37], v[144:145], v[132:133], v[36:37] op_sel_hi:[1,0,1]
	v_pk_fma_f32 v[38:39], v[132:133], v[146:147], v[38:39] op_sel_hi:[0,1,1]
	v_mov_b32_e32 v126, v113
	v_mov_b32_e32 v130, v115
	v_mov_b32_e32 v136, v117
	v_mov_b32_e32 v137, v119
	v_pk_fma_f32 v[32:33], v[156:157], v[120:121], v[32:33] op_sel_hi:[1,0,1]
	v_pk_fma_f32 v[34:35], v[120:121], v[158:159], v[34:35] op_sel_hi:[0,1,1]
	v_mov_b32_e32 v127, v37
	v_mov_b32_e32 v131, v39
	v_mov_b32_e32 v124, v112
	v_mov_b32_e32 v128, v114
	v_mov_b32_e32 v134, v116
	v_mov_b32_e32 v135, v118
	v_pk_mul_f32 v[136:137], v[136:137], v[136:137]
	v_pk_fma_f32 v[32:33], v[160:161], v[122:123], v[32:33] op_sel_hi:[1,0,1]
	v_pk_fma_f32 v[34:35], v[122:123], v[162:163], v[34:35] op_sel_hi:[0,1,1]
	v_mov_b32_e32 v125, v36
	v_mov_b32_e32 v129, v38
	v_pk_mul_f32 v[126:127], v[126:127], v[126:127]
	v_pk_mul_f32 v[130:131], v[130:131], v[130:131]
	v_pk_fma_f32 v[134:135], v[134:135], v[134:135], v[136:137]
	v_pk_fma_f32 v[32:33], v[164:165], v[132:133], v[32:33] op_sel_hi:[1,0,1]
	v_pk_fma_f32 v[34:35], v[132:133], v[166:167], v[34:35] op_sel_hi:[0,1,1]
	v_pk_fma_f32 v[124:125], v[124:125], v[124:125], v[126:127]
	v_pk_fma_f32 v[126:127], v[128:129], v[128:129], v[130:131]
	v_pk_fma_f32 v[96:97], v[168:169], v[132:133], v[96:97] op_sel_hi:[1,0,1]
	v_pk_fma_f32 v[98:99], v[132:133], v[170:171], v[98:99] op_sel_hi:[0,1,1]
	v_pk_fma_f32 v[100:101], v[172:173], v[132:133], v[100:101] op_sel_hi:[1,0,1]
	v_pk_fma_f32 v[102:103], v[132:133], v[174:175], v[102:103] op_sel_hi:[0,1,1]
	v_pk_fma_f32 v[104:105], v[176:177], v[132:133], v[104:105] op_sel_hi:[1,0,1]
	v_pk_fma_f32 v[106:107], v[132:133], v[178:179], v[106:107] op_sel_hi:[0,1,1]
	v_pk_fma_f32 v[108:109], v[180:181], v[132:133], v[108:109] op_sel_hi:[1,0,1]
	v_pk_fma_f32 v[110:111], v[132:133], v[182:183], v[110:111] op_sel_hi:[0,1,1]
	v_pk_add_f32 v[132:133], v[134:135], v[134:135] op_sel:[0,1] op_sel_hi:[1,0]
	v_mul_f32_e32 v134, v33, v33
	v_mul_f32_e32 v136, v35, v35
	v_pk_add_f32 v[124:125], v[124:125], v[126:127]
	v_pk_mul_f32 v[120:121], v[96:97], v[96:97]
	v_pk_mul_f32 v[138:139], v[98:99], v[98:99]
	v_pk_fma_f32 v[134:135], v[32:33], v[32:33], v[134:135] op_sel_hi:[1,1,0]
	v_pk_fma_f32 v[136:137], v[34:35], v[34:35], v[136:137] op_sel_hi:[1,1,0]
	v_pk_add_f32 v[124:125], v[124:125], v[124:125] op_sel:[0,1] op_sel_hi:[1,0]
	v_mov_b32_e32 v150, v101
	v_mov_b32_e32 v151, v103
	v_mov_b32_e32 v133, v121
	v_mov_b32_e32 v135, v138
	v_mov_b32_e32 v137, v139
	v_mov_b32_e32 v125, v120
	v_mov_b32_e32 v148, v100
	v_mov_b32_e32 v149, v102
	v_pk_mul_f32 v[122:123], v[150:151], v[150:151]
	v_pk_add_f32 v[126:127], v[134:135], v[136:137]
	v_pk_add_f32 v[120:121], v[124:125], v[132:133]
	v_mul_f32_e32 v152, v105, v105
	v_mul_f32_e32 v154, v107, v107
	v_pk_fma_f32 v[122:123], v[148:149], v[148:149], v[122:123]
	v_pk_add_f32 v[120:121], v[120:121], v[126:127]
	v_pk_mul_f32 v[156:157], v[108:109], v[108:109]
	v_pk_mul_f32 v[158:159], v[110:111], v[110:111]
	v_pk_fma_f32 v[140:141], v[104:105], v[104:105], v[152:153] op_sel_hi:[1,1,0]
	v_pk_fma_f32 v[142:143], v[106:107], v[106:107], v[154:155] op_sel_hi:[1,1,0]
	v_pk_add_f32 v[122:123], v[122:123], v[122:123] op_sel:[0,1] op_sel_hi:[1,0]
	v_pk_add_f32 v[120:121], v[120:121], v[120:121] op_sel:[0,1] op_sel_hi:[1,0]
	v_mov_b32_e32 v141, v158
	v_mov_b32_e32 v143, v159
	v_mov_b32_e32 v123, v157
	v_mov_b32_e32 v121, v156
	v_pk_add_f32 v[140:141], v[140:141], v[142:143]
	v_pk_add_f32 v[120:121], v[120:121], v[122:123]
	s_nop 0
	v_pk_add_f32 v[120:121], v[120:121], v[140:141]
	s_nop 0
	v_add_f32_e32 v120, v120, v121
	ds_bpermute_b32 v121, v88, v120
	s_waitcnt lgkmcnt(0)
; __global__ void __launch_bounds__(NTHR, 2) fwd(Args args) {
;     ...
;             const float r = rsqrtf(wave_sum(s) * (1.f / D) + EPS);
; #pragma unroll
;             for (int j = 0; j < 8; ++j) { const int cidx = (j * 64 + lane) * 4; *(f32x4*)(out + (size_t)t * D + cidx) = v[j] * r * fg[j]; }
	v_add_f32_e32 v120, v120, v121
	ds_bpermute_b32 v121, v89, v120
	s_waitcnt lgkmcnt(0)
	v_add_f32_e32 v120, v120, v121
	ds_bpermute_b32 v121, v90, v120
	s_waitcnt lgkmcnt(0)
	v_add_f32_e32 v120, v120, v121
	ds_bpermute_b32 v121, v91, v120
	s_waitcnt lgkmcnt(0)
	v_add_f32_e32 v120, v120, v121
	ds_bpermute_b32 v121, v92, v120
	s_waitcnt lgkmcnt(0)
	v_add_f32_e32 v120, v120, v121
	ds_bpermute_b32 v121, v93, v120
	s_waitcnt lgkmcnt(0)
	v_add_f32_e32 v120, v120, v121
	v_fmamk_f32 v120, v120, 0x3a000000, v95
	v_mul_f32_e32 v121, 0x4b800000, v120
	v_cmp_gt_f32_e32 vcc, s18, v120
	s_nop 1
	v_cndmask_b32_e32 v120, v120, v121, vcc
	v_rsq_f32_e32 v120, v120
	s_nop 0
	v_mul_f32_e32 v121, 0x45800000, v120
	v_cndmask_b32_e32 v120, v120, v121, vcc
	v_pk_mul_f32 v[112:113], v[120:121], v[112:113] op_sel_hi:[0,1]
	v_pk_mul_f32 v[114:115], v[120:121], v[114:115] op_sel_hi:[0,1]
	v_pk_mul_f32 v[36:37], v[120:121], v[36:37] op_sel_hi:[0,1]
	v_pk_mul_f32 v[38:39], v[120:121], v[38:39] op_sel_hi:[0,1]
	v_pk_mul_f32 v[116:117], v[120:121], v[116:117] op_sel_hi:[0,1]
	v_pk_mul_f32 v[118:119], v[120:121], v[118:119] op_sel_hi:[0,1]
	v_pk_mul_f32 v[122:123], v[120:121], v[32:33] op_sel_hi:[0,1]
	v_pk_mul_f32 v[124:125], v[120:121], v[34:35] op_sel_hi:[0,1]
	v_pk_mul_f32 v[126:127], v[120:121], v[96:97] op_sel_hi:[0,1]
	v_pk_mul_f32 v[128:129], v[120:121], v[98:99] op_sel_hi:[0,1]
	v_pk_mul_f32 v[130:131], v[120:121], v[100:101] op_sel_hi:[0,1]
	v_pk_mul_f32 v[132:133], v[120:121], v[102:103] op_sel_hi:[0,1]
	v_pk_mul_f32 v[134:135], v[120:121], v[104:105] op_sel_hi:[0,1]
	v_pk_mul_f32 v[136:137], v[120:121], v[106:107] op_sel_hi:[0,1]
	v_pk_mul_f32 v[138:139], v[120:121], v[108:109] op_sel_hi:[0,1]
	v_pk_mul_f32 v[120:121], v[120:121], v[110:111] op_sel_hi:[0,1]
	v_pk_mul_f32 v[34:35], v[114:115], v[2:3]
	v_pk_mul_f32 v[32:33], v[112:113], v[0:1]
	v_pk_mul_f32 v[38:39], v[38:39], v[6:7]
	v_pk_mul_f32 v[36:37], v[36:37], v[4:5]
	v_pk_mul_f32 v[98:99], v[118:119], v[10:11]
	v_pk_mul_f32 v[96:97], v[116:117], v[8:9]
	v_pk_mul_f32 v[102:103], v[124:125], v[14:15]
	v_pk_mul_f32 v[100:101], v[122:123], v[12:13]
	v_pk_mul_f32 v[106:107], v[128:129], v[18:19]
	v_pk_mul_f32 v[104:105], v[126:127], v[16:17]
	v_pk_mul_f32 v[110:111], v[132:133], v[22:23]
	v_pk_mul_f32 v[108:109], v[130:131], v[20:21]
	v_pk_mul_f32 v[114:115], v[136:137], v[26:27]
	v_pk_mul_f32 v[112:113], v[134:135], v[24:25]
	v_pk_mul_f32 v[118:119], v[120:121], v[30:31]
	v_pk_mul_f32 v[116:117], v[138:139], v[28:29]
	global_store_dwordx4 v[76:77], v[32:35], off
	global_store_dwordx4 v[76:77], v[36:39], off offset:1024
	global_store_dwordx4 v[76:77], v[96:99], off offset:2048
	global_store_dwordx4 v[76:77], v[100:103], off offset:3072
	global_store_dwordx4 v[78:79], v[104:107], off
	global_store_dwordx4 v[80:81], v[108:111], off
	global_store_dwordx4 v[82:83], v[112:115], off
	global_store_dwordx4 v[84:85], v[116:119], off
	v_mov_b32_e32 v184, v196
	v_mov_b32_e32 v185, v197
	v_mov_b32_e32 v186, v198
	v_mov_b32_e32 v187, v199
	v_mov_b32_e32 v188, v200
	v_mov_b32_e32 v189, v201
	v_mov_b32_e32 v190, v202
	v_mov_b32_e32 v191, v203
	v_mov_b32_e32 v192, v204
	v_mov_b32_e32 v193, v205
	v_mov_b32_e32 v194, v206
	v_mov_b32_e32 v195, v207
	v_mov_b32_e32 v196, v208
	v_mov_b32_e32 v197, v209
	v_mov_b32_e32 v198, v210
	v_mov_b32_e32 v199, v211
	v_mov_b32_e32 v200, v212
	v_mov_b32_e32 v201, v213
	v_mov_b32_e32 v202, v214
	v_mov_b32_e32 v203, v215
	v_mov_b32_e32 v204, v216
	v_mov_b32_e32 v205, v217
	v_mov_b32_e32 v206, v218
	v_mov_b32_e32 v207, v219
	v_mov_b32_e32 v208, v220
	v_mov_b32_e32 v209, v221
	v_mov_b32_e32 v210, v222
	v_mov_b32_e32 v211, v223
	v_mov_b32_e32 v212, v224
	v_mov_b32_e32 v213, v225
	v_mov_b32_e32 v214, v226
	v_mov_b32_e32 v215, v227
	v_mov_b32_e32 v216, v228
	v_mov_b32_e32 v217, v229
	v_mov_b32_e32 v218, v230
	v_mov_b32_e32 v219, v231
	s_cbranch_scc1 .LBB0_1674
